# baseline (speedup 1.0000x reference)
.LBB2_3:
	s_load_dwordx4 s[4:7], s[0:1], 0x10
	v_and_b32_e32 v51, 31, v1
	v_lshrrev_b32_e32 v50, 5, v1
	v_bfe_u32 v52, v1, 1, 3
	s_lshl_b32 s2, s13, 5
	v_or_b32_e32 v53, s2, v51
	v_lshlrev_b32_e32 v53, 7, v53
	v_add_u32_e32 v53, 0x800, v53
	v_lshlrev_b32_e32 v54, 7, v51
	v_add_u32_e32 v54, 0x4800, v54
	v_xor_b32_e32 v55, v50, v52
	v_lshlrev_b32_e32 v104, 4, v55
	v_add_u32_e32 v56, v53, v104
	v_add_u32_e32 v60, v54, v104
	v_add_u32_e32 v64, 0xe000, v56
	v_add_u32_e32 v68, 0xe000, v60
	v_add_u32_e32 v136, 0x1c000, v56
	v_add_u32_e32 v140, 0x1c000, v60
	v_xor_b32_e32 v104, 2, v55
	v_lshlrev_b32_e32 v104, 4, v104
	v_add_u32_e32 v57, v53, v104
	v_add_u32_e32 v61, v54, v104
	v_add_u32_e32 v65, 0xe000, v57
	v_add_u32_e32 v69, 0xe000, v61
	v_add_u32_e32 v137, 0x1c000, v57
	v_add_u32_e32 v141, 0x1c000, v61
	v_xor_b32_e32 v104, 4, v55
	v_lshlrev_b32_e32 v104, 4, v104
	v_add_u32_e32 v58, v53, v104
	v_add_u32_e32 v62, v54, v104
	v_add_u32_e32 v66, 0xe000, v58
	v_add_u32_e32 v70, 0xe000, v62
	v_add_u32_e32 v138, 0x1c000, v58
	v_add_u32_e32 v142, 0x1c000, v62
	v_xor_b32_e32 v104, 6, v55
	v_lshlrev_b32_e32 v104, 4, v104
	v_add_u32_e32 v59, v53, v104
	v_add_u32_e32 v63, v54, v104
	v_add_u32_e32 v67, 0xe000, v59
	v_add_u32_e32 v71, 0xe000, v63
	v_add_u32_e32 v139, 0x1c000, v59
	v_add_u32_e32 v143, 0x1c000, v63
	v_add_u32_e32 v104, s9, v51
	v_lshlrev_b32_e32 v104, 2, v104
	s_waitcnt lgkmcnt(0)
	global_load_dword v105, v104, s[4:5]
	global_load_dword v106, v104, s[4:5] offset:128
	global_load_dword v107, v104, s[4:5] offset:256
	s_waitcnt vmcnt(0)
	v_mov_b32_e32 v34, v105
	v_mov_b32_e32 v35, v105
	v_mov_b32_e32 v36, v105
	v_mov_b32_e32 v37, v105
	v_mov_b32_e32 v38, v105
	v_mov_b32_e32 v39, v105
	v_mov_b32_e32 v40, v105
	v_mov_b32_e32 v41, v105
	v_mov_b32_e32 v42, v105
	v_mov_b32_e32 v43, v105
	v_mov_b32_e32 v44, v105
	v_mov_b32_e32 v45, v105
	v_mov_b32_e32 v46, v105
	v_mov_b32_e32 v47, v105
	v_mov_b32_e32 v48, v105
	v_mov_b32_e32 v49, v105
	v_mov_b32_e32 v18, v106
	v_mov_b32_e32 v19, v106
	v_mov_b32_e32 v20, v106
	v_mov_b32_e32 v21, v106
	v_mov_b32_e32 v22, v106
	v_mov_b32_e32 v23, v106
	v_mov_b32_e32 v24, v106
	v_mov_b32_e32 v25, v106
	v_mov_b32_e32 v26, v106
	v_mov_b32_e32 v27, v106
	v_mov_b32_e32 v28, v106
	v_mov_b32_e32 v29, v106
	v_mov_b32_e32 v30, v106
	v_mov_b32_e32 v31, v106
	v_mov_b32_e32 v32, v106
	v_mov_b32_e32 v33, v106
	v_mov_b32_e32 v2, v107
	v_mov_b32_e32 v3, v107
	v_mov_b32_e32 v4, v107
	v_mov_b32_e32 v5, v107
	v_mov_b32_e32 v6, v107
	v_mov_b32_e32 v7, v107
	v_mov_b32_e32 v8, v107
	v_mov_b32_e32 v9, v107
	v_mov_b32_e32 v10, v107
	v_mov_b32_e32 v11, v107
	v_mov_b32_e32 v12, v107
	v_mov_b32_e32 v13, v107
	v_mov_b32_e32 v14, v107
	v_mov_b32_e32 v15, v107
	v_mov_b32_e32 v16, v107
	v_mov_b32_e32 v17, v107
	s_barrier
	ds_read_b128 v[72:75], v56
	ds_read_b128 v[76:79], v60
	ds_read_b128 v[80:83], v60 offset:4096
	ds_read_b128 v[84:87], v60 offset:8192
	ds_read_b128 v[88:91], v57
	ds_read_b128 v[92:95], v61
	ds_read_b128 v[96:99], v61 offset:4096
	ds_read_b128 v[100:103], v61 offset:8192
	s_waitcnt lgkmcnt(0)
	v_mfma_f32_32x32x16_f16 v[34:49], v[72:75], v[76:79], v[34:49]
	ds_read_b128 v[104:107], v58
	ds_read_b128 v[108:111], v62
	v_mfma_f32_32x32x16_f16 v[18:33], v[72:75], v[80:83], v[18:33]
	ds_read_b128 v[112:115], v62 offset:4096
	ds_read_b128 v[116:119], v62 offset:8192
	v_mfma_f32_32x32x16_f16 v[2:17], v[72:75], v[84:87], v[2:17]
	ds_read_b128 v[120:123], v59
	ds_read_b128 v[124:127], v63
	v_mfma_f32_32x32x16_f16 v[34:49], v[88:91], v[92:95], v[34:49]
	ds_read_b128 v[128:131], v63 offset:4096
	ds_read_b128 v[132:135], v63 offset:8192
	v_mfma_f32_32x32x16_f16 v[18:33], v[88:91], v[96:99], v[18:33]
	v_mfma_f32_32x32x16_f16 v[2:17], v[88:91], v[100:103], v[2:17]
	s_waitcnt lgkmcnt(0)
	s_barrier
	v_mfma_f32_32x32x16_f16 v[34:49], v[104:107], v[108:111], v[34:49]
	ds_read_b128 v[72:75], v56 offset:28672
	ds_read_b128 v[76:79], v60 offset:28672
	v_mfma_f32_32x32x16_f16 v[18:33], v[104:107], v[112:115], v[18:33]
	ds_read_b128 v[80:83], v60 offset:32768
	ds_read_b128 v[84:87], v60 offset:36864
	v_mfma_f32_32x32x16_f16 v[2:17], v[104:107], v[116:119], v[2:17]
	ds_read_b128 v[88:91], v57 offset:28672
	ds_read_b128 v[92:95], v61 offset:28672
	v_mfma_f32_32x32x16_f16 v[34:49], v[120:123], v[124:127], v[34:49]
	ds_read_b128 v[96:99], v61 offset:32768
	ds_read_b128 v[100:103], v61 offset:36864
	v_mfma_f32_32x32x16_f16 v[18:33], v[120:123], v[128:131], v[18:33]
	v_mfma_f32_32x32x16_f16 v[2:17], v[120:123], v[132:135], v[2:17]
	s_waitcnt lgkmcnt(0)
	v_mfma_f32_32x32x16_f16 v[34:49], v[72:75], v[76:79], v[34:49]
	ds_read_b128 v[104:107], v58 offset:28672
	ds_read_b128 v[108:111], v62 offset:28672
	v_mfma_f32_32x32x16_f16 v[18:33], v[72:75], v[80:83], v[18:33]
	ds_read_b128 v[112:115], v62 offset:32768
	ds_read_b128 v[116:119], v62 offset:36864
	v_mfma_f32_32x32x16_f16 v[2:17], v[72:75], v[84:87], v[2:17]
	ds_read_b128 v[120:123], v59 offset:28672
	ds_read_b128 v[124:127], v63 offset:28672
	v_mfma_f32_32x32x16_f16 v[34:49], v[88:91], v[92:95], v[34:49]
	ds_read_b128 v[128:131], v63 offset:32768
	ds_read_b128 v[132:135], v63 offset:36864
	v_mfma_f32_32x32x16_f16 v[18:33], v[88:91], v[96:99], v[18:33]
	v_mfma_f32_32x32x16_f16 v[2:17], v[88:91], v[100:103], v[2:17]
	s_waitcnt lgkmcnt(0)
	s_barrier
	v_mfma_f32_32x32x16_f16 v[34:49], v[104:107], v[108:111], v[34:49]
	ds_read_b128 v[72:75], v64
	ds_read_b128 v[76:79], v68
	v_mfma_f32_32x32x16_f16 v[18:33], v[104:107], v[112:115], v[18:33]
	ds_read_b128 v[80:83], v68 offset:4096
	ds_read_b128 v[84:87], v68 offset:8192
	v_mfma_f32_32x32x16_f16 v[2:17], v[104:107], v[116:119], v[2:17]
	ds_read_b128 v[88:91], v65
	ds_read_b128 v[92:95], v69
	v_mfma_f32_32x32x16_f16 v[34:49], v[120:123], v[124:127], v[34:49]
	ds_read_b128 v[96:99], v69 offset:4096
	ds_read_b128 v[100:103], v69 offset:8192
	v_mfma_f32_32x32x16_f16 v[18:33], v[120:123], v[128:131], v[18:33]
	v_mfma_f32_32x32x16_f16 v[2:17], v[120:123], v[132:135], v[2:17]
	s_waitcnt lgkmcnt(0)
	v_mfma_f32_32x32x16_f16 v[34:49], v[72:75], v[76:79], v[34:49]
	ds_read_b128 v[104:107], v66
	ds_read_b128 v[108:111], v70
	v_mfma_f32_32x32x16_f16 v[18:33], v[72:75], v[80:83], v[18:33]
	ds_read_b128 v[112:115], v70 offset:4096
	ds_read_b128 v[116:119], v70 offset:8192
	v_mfma_f32_32x32x16_f16 v[2:17], v[72:75], v[84:87], v[2:17]
	ds_read_b128 v[120:123], v67
	ds_read_b128 v[124:127], v71
	v_mfma_f32_32x32x16_f16 v[34:49], v[88:91], v[92:95], v[34:49]
	ds_read_b128 v[128:131], v71 offset:4096
	ds_read_b128 v[132:135], v71 offset:8192
	v_mfma_f32_32x32x16_f16 v[18:33], v[88:91], v[96:99], v[18:33]
	v_mfma_f32_32x32x16_f16 v[2:17], v[88:91], v[100:103], v[2:17]
	s_waitcnt lgkmcnt(0)
	s_barrier
	v_mfma_f32_32x32x16_f16 v[34:49], v[104:107], v[108:111], v[34:49]
	ds_read_b128 v[72:75], v64 offset:28672
	ds_read_b128 v[76:79], v68 offset:28672
	v_mfma_f32_32x32x16_f16 v[18:33], v[104:107], v[112:115], v[18:33]
	ds_read_b128 v[80:83], v68 offset:32768
	ds_read_b128 v[84:87], v68 offset:36864
	v_mfma_f32_32x32x16_f16 v[2:17], v[104:107], v[116:119], v[2:17]
	ds_read_b128 v[88:91], v65 offset:28672
	ds_read_b128 v[92:95], v69 offset:28672
	v_mfma_f32_32x32x16_f16 v[34:49], v[120:123], v[124:127], v[34:49]
	ds_read_b128 v[96:99], v69 offset:32768
	ds_read_b128 v[100:103], v69 offset:36864
	v_mfma_f32_32x32x16_f16 v[18:33], v[120:123], v[128:131], v[18:33]
	v_mfma_f32_32x32x16_f16 v[2:17], v[120:123], v[132:135], v[2:17]
	s_waitcnt lgkmcnt(0)
	v_mfma_f32_32x32x16_f16 v[34:49], v[72:75], v[76:79], v[34:49]
	ds_read_b128 v[104:107], v66 offset:28672
	ds_read_b128 v[108:111], v70 offset:28672
	v_mfma_f32_32x32x16_f16 v[18:33], v[72:75], v[80:83], v[18:33]
	ds_read_b128 v[112:115], v70 offset:32768
	ds_read_b128 v[116:119], v70 offset:36864
	v_mfma_f32_32x32x16_f16 v[2:17], v[72:75], v[84:87], v[2:17]
	ds_read_b128 v[120:123], v67 offset:28672
	ds_read_b128 v[124:127], v71 offset:28672
	v_mfma_f32_32x32x16_f16 v[34:49], v[88:91], v[92:95], v[34:49]
	ds_read_b128 v[128:131], v71 offset:32768
	ds_read_b128 v[132:135], v71 offset:36864
	v_mfma_f32_32x32x16_f16 v[18:33], v[88:91], v[96:99], v[18:33]
	v_mfma_f32_32x32x16_f16 v[2:17], v[88:91], v[100:103], v[2:17]
	s_waitcnt lgkmcnt(0)
	s_barrier
	v_mfma_f32_32x32x16_f16 v[34:49], v[104:107], v[108:111], v[34:49]
	ds_read_b128 v[72:75], v136
	ds_read_b128 v[76:79], v140
	v_mfma_f32_32x32x16_f16 v[18:33], v[104:107], v[112:115], v[18:33]
	ds_read_b128 v[80:83], v140 offset:4096
	ds_read_b128 v[84:87], v140 offset:8192
	v_mfma_f32_32x32x16_f16 v[2:17], v[104:107], v[116:119], v[2:17]
	ds_read_b128 v[88:91], v137
	ds_read_b128 v[92:95], v141
	v_mfma_f32_32x32x16_f16 v[34:49], v[120:123], v[124:127], v[34:49]
	ds_read_b128 v[96:99], v141 offset:4096
	ds_read_b128 v[100:103], v141 offset:8192
	v_mfma_f32_32x32x16_f16 v[18:33], v[120:123], v[128:131], v[18:33]
	v_mfma_f32_32x32x16_f16 v[2:17], v[120:123], v[132:135], v[2:17]
	s_waitcnt lgkmcnt(0)
	v_mfma_f32_32x32x16_f16 v[34:49], v[72:75], v[76:79], v[34:49]
	ds_read_b128 v[104:107], v138
	ds_read_b128 v[108:111], v142
	v_mfma_f32_32x32x16_f16 v[18:33], v[72:75], v[80:83], v[18:33]
	ds_read_b128 v[112:115], v142 offset:4096
	ds_read_b128 v[116:119], v142 offset:8192
	v_mfma_f32_32x32x16_f16 v[2:17], v[72:75], v[84:87], v[2:17]
	ds_read_b128 v[120:123], v139
	ds_read_b128 v[124:127], v143
	v_mfma_f32_32x32x16_f16 v[34:49], v[88:91], v[92:95], v[34:49]
	ds_read_b128 v[128:131], v143 offset:4096
	ds_read_b128 v[132:135], v143 offset:8192
	v_mfma_f32_32x32x16_f16 v[18:33], v[88:91], v[96:99], v[18:33]
	v_mfma_f32_32x32x16_f16 v[2:17], v[88:91], v[100:103], v[2:17]
	s_waitcnt lgkmcnt(0)
	s_barrier
	v_mfma_f32_32x32x16_f16 v[34:49], v[104:107], v[108:111], v[34:49]
	ds_read_b128 v[72:75], v56
	ds_read_b128 v[76:79], v60
	v_mfma_f32_32x32x16_f16 v[18:33], v[104:107], v[112:115], v[18:33]
	ds_read_b128 v[80:83], v60 offset:4096
	ds_read_b128 v[84:87], v60 offset:8192
	v_mfma_f32_32x32x16_f16 v[2:17], v[104:107], v[116:119], v[2:17]
	ds_read_b128 v[88:91], v57
	ds_read_b128 v[92:95], v61
	v_mfma_f32_32x32x16_f16 v[34:49], v[120:123], v[124:127], v[34:49]
	ds_read_b128 v[96:99], v61 offset:4096
	ds_read_b128 v[100:103], v61 offset:8192
	v_mfma_f32_32x32x16_f16 v[18:33], v[120:123], v[128:131], v[18:33]
	v_mfma_f32_32x32x16_f16 v[2:17], v[120:123], v[132:135], v[2:17]
	s_waitcnt lgkmcnt(0)
	v_mfma_f32_32x32x16_f16 v[34:49], v[72:75], v[76:79], v[34:49]
	ds_read_b128 v[104:107], v58
	ds_read_b128 v[108:111], v62
	v_mfma_f32_32x32x16_f16 v[18:33], v[72:75], v[80:83], v[18:33]
	ds_read_b128 v[112:115], v62 offset:4096
	ds_read_b128 v[116:119], v62 offset:8192
	v_mfma_f32_32x32x16_f16 v[2:17], v[72:75], v[84:87], v[2:17]
	ds_read_b128 v[120:123], v59
	ds_read_b128 v[124:127], v63
	v_mfma_f32_32x32x16_f16 v[34:49], v[88:91], v[92:95], v[34:49]
	ds_read_b128 v[128:131], v63 offset:4096
	ds_read_b128 v[132:135], v63 offset:8192
	v_mfma_f32_32x32x16_f16 v[18:33], v[88:91], v[96:99], v[18:33]
	v_mfma_f32_32x32x16_f16 v[2:17], v[88:91], v[100:103], v[2:17]
	s_waitcnt lgkmcnt(0)
	s_barrier
	v_mfma_f32_32x32x16_f16 v[34:49], v[104:107], v[108:111], v[34:49]
	ds_read_b128 v[72:75], v56 offset:28672
	ds_read_b128 v[76:79], v60 offset:28672
	v_mfma_f32_32x32x16_f16 v[18:33], v[104:107], v[112:115], v[18:33]
	ds_read_b128 v[80:83], v60 offset:32768
	ds_read_b128 v[84:87], v60 offset:36864
	v_mfma_f32_32x32x16_f16 v[2:17], v[104:107], v[116:119], v[2:17]
	ds_read_b128 v[88:91], v57 offset:28672
	ds_read_b128 v[92:95], v61 offset:28672
	v_mfma_f32_32x32x16_f16 v[34:49], v[120:123], v[124:127], v[34:49]
	ds_read_b128 v[96:99], v61 offset:32768
	ds_read_b128 v[100:103], v61 offset:36864
	v_mfma_f32_32x32x16_f16 v[18:33], v[120:123], v[128:131], v[18:33]
	v_mfma_f32_32x32x16_f16 v[2:17], v[120:123], v[132:135], v[2:17]
	s_waitcnt lgkmcnt(0)
	v_mfma_f32_32x32x16_f16 v[34:49], v[72:75], v[76:79], v[34:49]
	ds_read_b128 v[104:107], v58 offset:28672
	ds_read_b128 v[108:111], v62 offset:28672
	v_mfma_f32_32x32x16_f16 v[18:33], v[72:75], v[80:83], v[18:33]
	ds_read_b128 v[112:115], v62 offset:32768
	ds_read_b128 v[116:119], v62 offset:36864
	v_mfma_f32_32x32x16_f16 v[2:17], v[72:75], v[84:87], v[2:17]
	ds_read_b128 v[120:123], v59 offset:28672
	ds_read_b128 v[124:127], v63 offset:28672
	v_mfma_f32_32x32x16_f16 v[34:49], v[88:91], v[92:95], v[34:49]
	ds_read_b128 v[128:131], v63 offset:32768
	ds_read_b128 v[132:135], v63 offset:36864
	v_mfma_f32_32x32x16_f16 v[18:33], v[88:91], v[96:99], v[18:33]
	v_mfma_f32_32x32x16_f16 v[2:17], v[88:91], v[100:103], v[2:17]
	s_waitcnt lgkmcnt(0)
	s_barrier
	v_mfma_f32_32x32x16_f16 v[34:49], v[104:107], v[108:111], v[34:49]
	ds_read_b128 v[72:75], v64
	ds_read_b128 v[76:79], v68
	v_mfma_f32_32x32x16_f16 v[18:33], v[104:107], v[112:115], v[18:33]
	ds_read_b128 v[80:83], v68 offset:4096
	ds_read_b128 v[84:87], v68 offset:8192
	v_mfma_f32_32x32x16_f16 v[2:17], v[104:107], v[116:119], v[2:17]
	ds_read_b128 v[88:91], v65
	ds_read_b128 v[92:95], v69
	v_mfma_f32_32x32x16_f16 v[34:49], v[120:123], v[124:127], v[34:49]
	ds_read_b128 v[96:99], v69 offset:4096
	ds_read_b128 v[100:103], v69 offset:8192
	v_mfma_f32_32x32x16_f16 v[18:33], v[120:123], v[128:131], v[18:33]
	v_mfma_f32_32x32x16_f16 v[2:17], v[120:123], v[132:135], v[2:17]
	s_waitcnt lgkmcnt(0)
	v_mfma_f32_32x32x16_f16 v[34:49], v[72:75], v[76:79], v[34:49]
	ds_read_b128 v[104:107], v66
	ds_read_b128 v[108:111], v70
	v_mfma_f32_32x32x16_f16 v[18:33], v[72:75], v[80:83], v[18:33]
	ds_read_b128 v[112:115], v70 offset:4096
	ds_read_b128 v[116:119], v70 offset:8192
	v_mfma_f32_32x32x16_f16 v[2:17], v[72:75], v[84:87], v[2:17]
	ds_read_b128 v[120:123], v67
	ds_read_b128 v[124:127], v71
	v_mfma_f32_32x32x16_f16 v[34:49], v[88:91], v[92:95], v[34:49]
	ds_read_b128 v[128:131], v71 offset:4096
	ds_read_b128 v[132:135], v71 offset:8192
	v_mfma_f32_32x32x16_f16 v[18:33], v[88:91], v[96:99], v[18:33]
	v_mfma_f32_32x32x16_f16 v[2:17], v[88:91], v[100:103], v[2:17]
	s_waitcnt lgkmcnt(0)
	s_barrier
	v_mfma_f32_32x32x16_f16 v[34:49], v[104:107], v[108:111], v[34:49]
	ds_read_b128 v[72:75], v64 offset:28672
	ds_read_b128 v[76:79], v68 offset:28672
	v_mfma_f32_32x32x16_f16 v[18:33], v[104:107], v[112:115], v[18:33]
	ds_read_b128 v[80:83], v68 offset:32768
	ds_read_b128 v[84:87], v68 offset:36864
	v_mfma_f32_32x32x16_f16 v[2:17], v[104:107], v[116:119], v[2:17]
	ds_read_b128 v[88:91], v65 offset:28672
	ds_read_b128 v[92:95], v69 offset:28672
	v_mfma_f32_32x32x16_f16 v[34:49], v[120:123], v[124:127], v[34:49]
	ds_read_b128 v[96:99], v69 offset:32768
	ds_read_b128 v[100:103], v69 offset:36864
	v_mfma_f32_32x32x16_f16 v[18:33], v[120:123], v[128:131], v[18:33]
	v_mfma_f32_32x32x16_f16 v[2:17], v[120:123], v[132:135], v[2:17]
	s_waitcnt lgkmcnt(0)
	v_mfma_f32_32x32x16_f16 v[34:49], v[72:75], v[76:79], v[34:49]
	ds_read_b128 v[104:107], v66 offset:28672
	ds_read_b128 v[108:111], v70 offset:28672
	v_mfma_f32_32x32x16_f16 v[18:33], v[72:75], v[80:83], v[18:33]
	ds_read_b128 v[112:115], v70 offset:32768
	ds_read_b128 v[116:119], v70 offset:36864
	v_mfma_f32_32x32x16_f16 v[2:17], v[72:75], v[84:87], v[2:17]
	ds_read_b128 v[120:123], v67 offset:28672
	ds_read_b128 v[124:127], v71 offset:28672
	v_mfma_f32_32x32x16_f16 v[34:49], v[88:91], v[92:95], v[34:49]
	ds_read_b128 v[128:131], v71 offset:32768
	ds_read_b128 v[132:135], v71 offset:36864
	v_mfma_f32_32x32x16_f16 v[18:33], v[88:91], v[96:99], v[18:33]
	v_mfma_f32_32x32x16_f16 v[2:17], v[88:91], v[100:103], v[2:17]
	s_waitcnt lgkmcnt(0)
	s_barrier
	v_mfma_f32_32x32x16_f16 v[34:49], v[104:107], v[108:111], v[34:49]
	ds_read_b128 v[72:75], v136
	ds_read_b128 v[76:79], v140
	v_mfma_f32_32x32x16_f16 v[18:33], v[104:107], v[112:115], v[18:33]
	ds_read_b128 v[80:83], v140 offset:4096
	ds_read_b128 v[84:87], v140 offset:8192
	v_mfma_f32_32x32x16_f16 v[2:17], v[104:107], v[116:119], v[2:17]
	ds_read_b128 v[88:91], v137
	ds_read_b128 v[92:95], v141
	v_mfma_f32_32x32x16_f16 v[34:49], v[120:123], v[124:127], v[34:49]
	ds_read_b128 v[96:99], v141 offset:4096
	ds_read_b128 v[100:103], v141 offset:8192
	v_mfma_f32_32x32x16_f16 v[18:33], v[120:123], v[128:131], v[18:33]
	v_mfma_f32_32x32x16_f16 v[2:17], v[120:123], v[132:135], v[2:17]
	s_waitcnt lgkmcnt(0)
	v_mfma_f32_32x32x16_f16 v[34:49], v[72:75], v[76:79], v[34:49]
	ds_read_b128 v[104:107], v138
	ds_read_b128 v[108:111], v142
	v_mfma_f32_32x32x16_f16 v[18:33], v[72:75], v[80:83], v[18:33]
	ds_read_b128 v[112:115], v142 offset:4096
	ds_read_b128 v[116:119], v142 offset:8192
	v_mfma_f32_32x32x16_f16 v[2:17], v[72:75], v[84:87], v[2:17]
	ds_read_b128 v[120:123], v139
	ds_read_b128 v[124:127], v143
	v_mfma_f32_32x32x16_f16 v[34:49], v[88:91], v[92:95], v[34:49]
	ds_read_b128 v[128:131], v143 offset:4096
	ds_read_b128 v[132:135], v143 offset:8192
	v_mfma_f32_32x32x16_f16 v[18:33], v[88:91], v[96:99], v[18:33]
	v_mfma_f32_32x32x16_f16 v[2:17], v[88:91], v[100:103], v[2:17]
	s_waitcnt lgkmcnt(0)
	s_barrier
	v_mfma_f32_32x32x16_f16 v[34:49], v[104:107], v[108:111], v[34:49]
	ds_read_b128 v[72:75], v56
	ds_read_b128 v[76:79], v60
	v_mfma_f32_32x32x16_f16 v[18:33], v[104:107], v[112:115], v[18:33]
	ds_read_b128 v[80:83], v60 offset:4096
	ds_read_b128 v[84:87], v60 offset:8192
	v_mfma_f32_32x32x16_f16 v[2:17], v[104:107], v[116:119], v[2:17]
	ds_read_b128 v[88:91], v57
	ds_read_b128 v[92:95], v61
	v_mfma_f32_32x32x16_f16 v[34:49], v[120:123], v[124:127], v[34:49]
	ds_read_b128 v[96:99], v61 offset:4096
	ds_read_b128 v[100:103], v61 offset:8192
	v_mfma_f32_32x32x16_f16 v[18:33], v[120:123], v[128:131], v[18:33]
	v_mfma_f32_32x32x16_f16 v[2:17], v[120:123], v[132:135], v[2:17]
	s_waitcnt lgkmcnt(0)
	v_mfma_f32_32x32x16_f16 v[34:49], v[72:75], v[76:79], v[34:49]
	ds_read_b128 v[104:107], v58
	ds_read_b128 v[108:111], v62
	v_mfma_f32_32x32x16_f16 v[18:33], v[72:75], v[80:83], v[18:33]
	ds_read_b128 v[112:115], v62 offset:4096
	ds_read_b128 v[116:119], v62 offset:8192
	v_mfma_f32_32x32x16_f16 v[2:17], v[72:75], v[84:87], v[2:17]
	ds_read_b128 v[120:123], v59
	ds_read_b128 v[124:127], v63
	v_mfma_f32_32x32x16_f16 v[34:49], v[88:91], v[92:95], v[34:49]
	ds_read_b128 v[128:131], v63 offset:4096
	ds_read_b128 v[132:135], v63 offset:8192
	v_mfma_f32_32x32x16_f16 v[18:33], v[88:91], v[96:99], v[18:33]
	v_mfma_f32_32x32x16_f16 v[2:17], v[88:91], v[100:103], v[2:17]
	s_waitcnt lgkmcnt(0)
	s_barrier
	v_mfma_f32_32x32x16_f16 v[34:49], v[104:107], v[108:111], v[34:49]
	ds_read_b128 v[72:75], v56 offset:28672
	ds_read_b128 v[76:79], v60 offset:28672
	v_mfma_f32_32x32x16_f16 v[18:33], v[104:107], v[112:115], v[18:33]
	ds_read_b128 v[80:83], v60 offset:32768
	ds_read_b128 v[84:87], v60 offset:36864
	v_mfma_f32_32x32x16_f16 v[2:17], v[104:107], v[116:119], v[2:17]
	ds_read_b128 v[88:91], v57 offset:28672
	ds_read_b128 v[92:95], v61 offset:28672
	v_mfma_f32_32x32x16_f16 v[34:49], v[120:123], v[124:127], v[34:49]
	ds_read_b128 v[96:99], v61 offset:32768
	ds_read_b128 v[100:103], v61 offset:36864
	v_mfma_f32_32x32x16_f16 v[18:33], v[120:123], v[128:131], v[18:33]
	v_mfma_f32_32x32x16_f16 v[2:17], v[120:123], v[132:135], v[2:17]
	s_waitcnt lgkmcnt(0)
	v_mfma_f32_32x32x16_f16 v[34:49], v[72:75], v[76:79], v[34:49]
	ds_read_b128 v[104:107], v58 offset:28672
	ds_read_b128 v[108:111], v62 offset:28672
	v_mfma_f32_32x32x16_f16 v[18:33], v[72:75], v[80:83], v[18:33]
	ds_read_b128 v[112:115], v62 offset:32768
	ds_read_b128 v[116:119], v62 offset:36864
	v_mfma_f32_32x32x16_f16 v[2:17], v[72:75], v[84:87], v[2:17]
	ds_read_b128 v[120:123], v59 offset:28672
	ds_read_b128 v[124:127], v63 offset:28672
	v_mfma_f32_32x32x16_f16 v[34:49], v[88:91], v[92:95], v[34:49]
	ds_read_b128 v[128:131], v63 offset:32768
	ds_read_b128 v[132:135], v63 offset:36864
	v_mfma_f32_32x32x16_f16 v[18:33], v[88:91], v[96:99], v[18:33]
	v_mfma_f32_32x32x16_f16 v[2:17], v[88:91], v[100:103], v[2:17]
	s_waitcnt lgkmcnt(0)
	v_mfma_f32_32x32x16_f16 v[34:49], v[104:107], v[108:111], v[34:49]
	v_mfma_f32_32x32x16_f16 v[18:33], v[104:107], v[112:115], v[18:33]
	v_mfma_f32_32x32x16_f16 v[2:17], v[104:107], v[116:119], v[2:17]
	v_mfma_f32_32x32x16_f16 v[34:49], v[120:123], v[124:127], v[34:49]
	v_mfma_f32_32x32x16_f16 v[18:33], v[120:123], v[128:131], v[18:33]
	v_mfma_f32_32x32x16_f16 v[2:17], v[120:123], v[132:135], v[2:17]
	v_add_u32_e32 v51, s9, v51
	v_lshlrev_b32_e32 v104, 2, v51
	s_add_i32 s2, s2, s8
	v_lshl_add_u32 v108, v50, 2, s2
	v_mul_u32_u24_e32 v108, 0xc00, v108
	v_add_u32_e32 v108, v108, v104
	s_nop 15
	global_store_dword v108, v34, s[6:7] nt
	global_store_dword v108, v18, s[6:7] offset:128 nt
	global_store_dword v108, v2, s[6:7] offset:256 nt
	v_add_u32_e32 v109, 0xc00, v108
	global_store_dword v109, v35, s[6:7] nt
	global_store_dword v109, v19, s[6:7] offset:128 nt
	global_store_dword v109, v3, s[6:7] offset:256 nt
	v_add_u32_e32 v109, 0x1800, v108
	global_store_dword v109, v36, s[6:7] nt
	global_store_dword v109, v20, s[6:7] offset:128 nt
	global_store_dword v109, v4, s[6:7] offset:256 nt
	v_add_u32_e32 v109, 0x2400, v108
	global_store_dword v109, v37, s[6:7] nt
	global_store_dword v109, v21, s[6:7] offset:128 nt
	global_store_dword v109, v5, s[6:7] offset:256 nt
	v_add_u32_e32 v109, 0x6000, v108
	global_store_dword v109, v38, s[6:7] nt
	global_store_dword v109, v22, s[6:7] offset:128 nt
	global_store_dword v109, v6, s[6:7] offset:256 nt
	v_add_u32_e32 v109, 0x6c00, v108
	global_store_dword v109, v39, s[6:7] nt
	global_store_dword v109, v23, s[6:7] offset:128 nt
	global_store_dword v109, v7, s[6:7] offset:256 nt
	v_add_u32_e32 v109, 0x7800, v108
	global_store_dword v109, v40, s[6:7] nt
	global_store_dword v109, v24, s[6:7] offset:128 nt
	global_store_dword v109, v8, s[6:7] offset:256 nt
	v_add_u32_e32 v109, 0x8400, v108
	global_store_dword v109, v41, s[6:7] nt
	global_store_dword v109, v25, s[6:7] offset:128 nt
	global_store_dword v109, v9, s[6:7] offset:256 nt
	v_add_u32_e32 v109, 0xc000, v108
	global_store_dword v109, v42, s[6:7] nt
	global_store_dword v109, v26, s[6:7] offset:128 nt
	global_store_dword v109, v10, s[6:7] offset:256 nt
	v_add_u32_e32 v109, 0xcc00, v108
	global_store_dword v109, v43, s[6:7] nt
	global_store_dword v109, v27, s[6:7] offset:128 nt
	global_store_dword v109, v11, s[6:7] offset:256 nt
	v_add_u32_e32 v109, 0xd800, v108
	global_store_dword v109, v44, s[6:7] nt
	global_store_dword v109, v28, s[6:7] offset:128 nt
	global_store_dword v109, v12, s[6:7] offset:256 nt
	v_add_u32_e32 v109, 0xe400, v108
	global_store_dword v109, v45, s[6:7] nt
	global_store_dword v109, v29, s[6:7] offset:128 nt
	global_store_dword v109, v13, s[6:7] offset:256 nt
	v_add_u32_e32 v109, 0x12000, v108
	global_store_dword v109, v46, s[6:7] nt
	global_store_dword v109, v30, s[6:7] offset:128 nt
	global_store_dword v109, v14, s[6:7] offset:256 nt
	v_add_u32_e32 v109, 0x12c00, v108
	global_store_dword v109, v47, s[6:7] nt
	global_store_dword v109, v31, s[6:7] offset:128 nt
	global_store_dword v109, v15, s[6:7] offset:256 nt
	v_add_u32_e32 v109, 0x13800, v108
	global_store_dword v109, v48, s[6:7] nt
	global_store_dword v109, v32, s[6:7] offset:128 nt
	global_store_dword v109, v16, s[6:7] offset:256 nt
	v_add_u32_e32 v109, 0x14400, v108
	global_store_dword v109, v49, s[6:7] nt
	global_store_dword v109, v33, s[6:7] offset:128 nt
	global_store_dword v109, v17, s[6:7] offset:256 nt
	s_endpgm
